# instruction selection: MoE accumulator init (bias fold) with v_mov_b64 pairs, lin bias+1 computed once (72 instead of 128 VALU per unit); on top of XCD-aware up map
# speedup vs baseline: 1.0015x; 1.0000x over previous
; template <class Epi, class Sched, bool ALIGN_EPI = false, bool SP2 = false, bool GATHER = false, bool HALFM = false>
; __device__ __forceinline__ void gemm_phase(PG8_LAS unsigned char* lds, const int Kdim, const Sched& S, const Epi& E) {
;     ...
;     f32x4 acc[2][2][4][2];
; #pragma unroll
;     for (int a = 0; a < 2; ++a)
; #pragma unroll
;         for (int b = 0; b < 2; ++b)
; #pragma unroll
;             for (int m = 0; m < 4; ++m)
; #pragma unroll
;                 for (int n = 0; n < 2; ++n) acc[a][b][m][n] = (f32x4){0.f, 0.f, 0.f, 0.f};
;     __device__ __forceinline__ void operator()(const pg8::f32x4 (&acc)[2][2][4][2], const pg8::Unit& u, int wr, int wc, int fr, int fq) const {
;     ...
;         const int colj = u.pn * 128 + wc * 32 + 8 * fq;
;         const float* bg = b_up + u.e * 2048 + colj;
;         f32x4 bgv[2], blv[2];
; #pragma unroll
;         for (int n = 0; n < 2; ++n) { bgv[n] = *(const f32x4*)(bg + 4 * n); blv[n] = *(const f32x4*)(bg + 1024 + 4 * n); }
.LBB0_1696:
	v_readlane_b32 s52, v251, 31
	s_lshl_b64 s[14:15], s[20:21], 18
	v_readlane_b32 s56, v251, 35
	v_bfe_u32 v9, v2, 4, 2
	v_readlane_b32 s57, v251, 36
	s_add_u32 s37, s56, s14
	v_and_b32_e32 v8, 15, v2
	v_lshlrev_b32_e32 v10, 3, v9
	v_lshlrev_b32_e32 v9, 4, v9
	v_lshlrev_b32_e32 v2, 2, v2
	s_addc_u32 s49, s57, s15
	s_and_b32 s7, s4, 3
	v_lshl_or_b32 v169, s5, 6, v8
	v_lshl_or_b32 v8, v8, 6, v9
	s_lshl_b32 s4, s5, 13
	v_and_b32_e32 v2, 32, v2
	v_bitop3_b32 v9, v8, s4, v2 bitop3:0xde
	s_lshl_b32 s4, s7, 12
	v_bitop3_b32 v170, v8, s4, v2 bitop3:0xde
	s_add_i32 m0, s12, 0x18000
	v_lshl_add_u64 v[4:5], v[4:5], 0, s[34:35]
	v_readlane_b32 s4, v251, 8
	v_mov_b32_e32 v149, v3
	s_waitcnt vmcnt(2)
	s_barrier
	global_load_lds_dwordx4 v[4:5], off
	v_lshl_add_u64 v[4:5], v[6:7], 0, s[34:35]
	s_add_i32 m0, s12, 0x1a000
	v_readlane_b32 s5, v251, 9
	s_add_i32 s50, s12, 0x8000
	v_mov_b32_e32 v151, v3
	global_load_lds_dwordx4 v[4:5], off
	v_lshl_add_u64 v[4:5], s[4:5], 0, v[148:149]
	s_mov_b32 m0, s50
	s_add_i32 s51, s12, 0xa000
	global_load_lds_dwordx4 v[4:5], off
	v_lshl_add_u64 v[4:5], s[4:5], 0, v[150:151]
	s_add_u32 s4, s40, 0x40080
	s_mov_b32 m0, s51
	s_addc_u32 s5, s41, 0
	global_load_lds_dwordx4 v[4:5], off
	s_add_i32 m0, s12, 0x1c000
	v_lshl_add_u64 v[4:5], s[4:5], 0, v[156:157]
	global_load_lds_dwordx4 v[4:5], off
	v_lshl_add_u64 v[4:5], s[4:5], 0, v[158:159]
	s_add_i32 m0, s12, 0x1e000
	s_cmpk_lt_u32 s6, 0x100
	global_load_lds_dwordx4 v[4:5], off
	s_waitcnt vmcnt(6)
	v_readlane_b32 s53, v251, 32
	v_readlane_b32 s54, v251, 33
	v_readlane_b32 s55, v251, 34
	v_lshl_or_b32 v149, s7, 5, v10
	s_cselect_b64 s[6:7], -1, 0
	s_lshl_b32 s4, s46, 11
	s_ashr_i32 s5, s4, 31
	s_lshl_b64 s[4:5], s[4:5], 2
	v_lshl_or_b32 v136, s47, 7, v149
	s_add_u32 s4, s37, s4
	s_addc_u32 s5, s49, s5
	v_ashrrev_i32_e32 v137, 31, v136
	v_lshl_add_u64 v[136:137], v[136:137], 2, s[4:5]
	global_load_dwordx4 v[224:227], v[136:137], off
	global_load_dwordx4 v[228:231], v[136:137], off offset:16
	s_mov_b64 s[4:5], 0x1000
	v_lshl_add_u64 v[138:139], v[136:137], 0, s[4:5]
	global_load_dwordx4 v[232:235], v[138:139], off
	global_load_dwordx4 v[236:239], v[138:139], off offset:16
	s_waitcnt vmcnt(0)
	v_add_f32_e32 v232, 1.0, v232
	v_add_f32_e32 v233, 1.0, v233
	v_add_f32_e32 v234, 1.0, v234
	v_add_f32_e32 v235, 1.0, v235
	v_add_f32_e32 v236, 1.0, v236
	v_add_f32_e32 v237, 1.0, v237
	v_add_f32_e32 v238, 1.0, v238
	v_add_f32_e32 v239, 1.0, v239
	v_or_b32_e32 v151, 16, v169
	v_or_b32_e32 v171, 32, v169
	v_or_b32_e32 v172, 48, v169
	v_add_u32_e32 v173, 0x80, v169
	v_add_u32_e32 v174, 0x90, v169
	v_add_u32_e32 v175, 0xa0, v169
	v_add_u32_e32 v176, 0xb0, v169
	s_mov_b32 s76, 0
	v_add_u32_e32 v177, 0, v9
	v_mov_b64_e32 v[4:5], v[236:237]
	v_mov_b64_e32 v[6:7], v[238:239]
	v_mov_b64_e32 v[8:9], v[232:233]
	v_mov_b64_e32 v[10:11], v[234:235]
	v_mov_b64_e32 v[12:13], v[236:237]
	v_mov_b64_e32 v[14:15], v[238:239]
	v_mov_b64_e32 v[16:17], v[232:233]
	v_mov_b64_e32 v[18:19], v[234:235]
	v_mov_b64_e32 v[20:21], v[236:237]
	v_mov_b64_e32 v[22:23], v[238:239]
	v_mov_b64_e32 v[24:25], v[232:233]
	v_mov_b64_e32 v[26:27], v[234:235]
	v_mov_b64_e32 v[28:29], v[236:237]
	v_mov_b64_e32 v[30:31], v[238:239]
	v_mov_b64_e32 v[32:33], v[232:233]
	v_mov_b64_e32 v[34:35], v[234:235]
	v_mov_b64_e32 v[36:37], v[228:229]
	v_mov_b64_e32 v[38:39], v[230:231]
	v_mov_b64_e32 v[40:41], v[224:225]
	v_mov_b64_e32 v[42:43], v[226:227]
	v_mov_b64_e32 v[44:45], v[228:229]
	v_mov_b64_e32 v[46:47], v[230:231]
	v_mov_b64_e32 v[48:49], v[224:225]
	v_mov_b64_e32 v[50:51], v[226:227]
	v_mov_b64_e32 v[52:53], v[228:229]
	v_mov_b64_e32 v[54:55], v[230:231]
	v_mov_b64_e32 v[56:57], v[224:225]
	v_mov_b64_e32 v[58:59], v[226:227]
	v_mov_b64_e32 v[60:61], v[228:229]
	v_mov_b64_e32 v[62:63], v[230:231]
	v_mov_b64_e32 v[64:65], v[224:225]
	v_mov_b64_e32 v[66:67], v[226:227]
	v_mov_b64_e32 v[68:69], v[236:237]
	v_mov_b64_e32 v[70:71], v[238:239]
	v_mov_b64_e32 v[72:73], v[232:233]
	v_mov_b64_e32 v[74:75], v[234:235]
	v_mov_b64_e32 v[76:77], v[236:237]
	v_mov_b64_e32 v[78:79], v[238:239]
	v_mov_b64_e32 v[80:81], v[232:233]
	v_mov_b64_e32 v[82:83], v[234:235]
	v_mov_b64_e32 v[84:85], v[236:237]
	v_mov_b64_e32 v[86:87], v[238:239]
	v_mov_b64_e32 v[88:89], v[232:233]
	v_mov_b64_e32 v[90:91], v[234:235]
	v_mov_b64_e32 v[92:93], v[236:237]
	v_mov_b64_e32 v[94:95], v[238:239]
	v_mov_b64_e32 v[96:97], v[232:233]
	v_mov_b64_e32 v[98:99], v[234:235]
	v_mov_b64_e32 v[100:101], v[228:229]
	v_mov_b64_e32 v[102:103], v[230:231]
	v_mov_b64_e32 v[104:105], v[224:225]
	v_mov_b64_e32 v[106:107], v[226:227]
	v_mov_b64_e32 v[108:109], v[228:229]
	v_mov_b64_e32 v[110:111], v[230:231]
	v_mov_b64_e32 v[112:113], v[224:225]
	v_mov_b64_e32 v[114:115], v[226:227]
	v_mov_b64_e32 v[116:117], v[228:229]
	v_mov_b64_e32 v[118:119], v[230:231]
	v_mov_b64_e32 v[120:121], v[224:225]
	v_mov_b64_e32 v[122:123], v[226:227]
	v_mov_b64_e32 v[124:125], v[228:229]
	v_mov_b64_e32 v[126:127], v[230:231]
	v_mov_b64_e32 v[128:129], v[224:225]
	v_mov_b64_e32 v[130:131], v[226:227]
	v_readlane_b32 s58, v251, 37
	v_readlane_b32 s59, v251, 38
	v_readlane_b32 s60, v251, 39
	v_readlane_b32 s61, v251, 40
	v_readlane_b32 s62, v251, 41
	v_readlane_b32 s63, v251, 42
	v_readlane_b32 s64, v251, 43
	v_readlane_b32 s65, v251, 44
	v_readlane_b32 s66, v251, 45
	v_readlane_b32 s67, v251, 46
	s_barrier
	s_branch .LBB0_1698
; template <class Epi, class Sched, bool ALIGN_EPI = false, bool SP2 = false, bool GATHER = false, bool HALFM = false>
; __device__ __forceinline__ void gemm_phase(PG8_LAS unsigned char* lds, const int Kdim, const Sched& S, const Epi& E) {
;     ...
; #pragma unroll
;         for (int a = 0; a < 2; ++a)
; #pragma unroll
;             for (int b = 0; b < 2; ++b)
; #pragma unroll
;                 for (int m = 0; m < 4; ++m)
; #pragma unroll
;                     for (int n = 0; n < 2; ++n) acc[a][b][m][n] = (f32x4){0.f, 0.f, 0.f, 0.f};
;         cur = nxt; cA = nA; cB = nB; ++ui;
;         if constexpr (GATHER) {
; #pragma unroll
;             for (int h = 0; h < 2; ++h)
; #pragma unroll
;                 for (int i = 0; i < 2; ++i) { gc[h][i] = gn[h][i]; if (has_nn) gn[h][i] = (unsigned)ix[h][i] * (unsigned)(K * 2) + CA2[i]; } }
.LBB0_1697:
	v_lshlrev_b32_e32 v178, 11, v178
	v_lshlrev_b32_e32 v179, 11, v179
	v_lshlrev_b32_e32 v180, 11, v180
	v_lshlrev_b32_e32 v181, 11, v181
	v_add_u32_e32 v4, v178, v165
	v_cndmask_b32_e64 v5, v166, v4, s[42:43]
	v_add_u32_e32 v4, v181, v162
	v_add_u32_e32 v2, v179, v162
	v_cndmask_b32_e64 v6, v167, v4, s[42:43]
	v_add_u32_e32 v4, v180, v165
	v_cndmask_b32_e64 v2, v163, v2, s[42:43]
	v_cndmask_b32_e64 v7, v168, v4, s[42:43]
	s_waitcnt vmcnt(8)
	v_add_f32_e32 v232, 1.0, v232
	v_add_f32_e32 v233, 1.0, v233
	v_add_f32_e32 v234, 1.0, v234
	v_add_f32_e32 v235, 1.0, v235
	v_add_f32_e32 v236, 1.0, v236
	v_add_f32_e32 v237, 1.0, v237
	v_add_f32_e32 v238, 1.0, v238
	v_add_f32_e32 v239, 1.0, v239
	v_mov_b32_e32 v148, v163
	v_mov_b32_e32 v150, v166
	v_mov_b32_e32 v152, v167
	v_mov_b32_e32 v154, v168
	v_mov_b32_e32 v163, v2
	v_mov_b32_e32 v166, v5
	v_mov_b32_e32 v167, v6
	v_mov_b32_e32 v168, v7
	s_mov_b32 s48, s57
	s_mov_b32 s47, s54
	s_mov_b32 s46, s52
	s_mov_b64 s[40:41], s[16:17]
	v_mov_b64_e32 v[4:5], v[236:237]
	v_mov_b64_e32 v[6:7], v[238:239]
	v_mov_b64_e32 v[8:9], v[232:233]
	v_mov_b64_e32 v[10:11], v[234:235]
	v_mov_b64_e32 v[12:13], v[236:237]
	v_mov_b64_e32 v[14:15], v[238:239]
	v_mov_b64_e32 v[16:17], v[232:233]
	v_mov_b64_e32 v[18:19], v[234:235]
	v_mov_b64_e32 v[20:21], v[236:237]
	v_mov_b64_e32 v[22:23], v[238:239]
	v_mov_b64_e32 v[24:25], v[232:233]
	v_mov_b64_e32 v[26:27], v[234:235]
	v_mov_b64_e32 v[28:29], v[236:237]
	v_mov_b64_e32 v[30:31], v[238:239]
	v_mov_b64_e32 v[32:33], v[232:233]
	v_mov_b64_e32 v[34:35], v[234:235]
	v_mov_b64_e32 v[36:37], v[228:229]
	v_mov_b64_e32 v[38:39], v[230:231]
	v_mov_b64_e32 v[40:41], v[224:225]
	v_mov_b64_e32 v[42:43], v[226:227]
	v_mov_b64_e32 v[44:45], v[228:229]
	v_mov_b64_e32 v[46:47], v[230:231]
	v_mov_b64_e32 v[48:49], v[224:225]
	v_mov_b64_e32 v[50:51], v[226:227]
	v_mov_b64_e32 v[52:53], v[228:229]
	v_mov_b64_e32 v[54:55], v[230:231]
	v_mov_b64_e32 v[56:57], v[224:225]
	v_mov_b64_e32 v[58:59], v[226:227]
	v_mov_b64_e32 v[60:61], v[228:229]
	v_mov_b64_e32 v[62:63], v[230:231]
	v_mov_b64_e32 v[64:65], v[224:225]
	v_mov_b64_e32 v[66:67], v[226:227]
	v_mov_b64_e32 v[68:69], v[236:237]
	v_mov_b64_e32 v[70:71], v[238:239]
	v_mov_b64_e32 v[72:73], v[232:233]
	v_mov_b64_e32 v[74:75], v[234:235]
	v_mov_b64_e32 v[76:77], v[236:237]
	v_mov_b64_e32 v[78:79], v[238:239]
	v_mov_b64_e32 v[80:81], v[232:233]
	v_mov_b64_e32 v[82:83], v[234:235]
	v_mov_b64_e32 v[84:85], v[236:237]
	v_mov_b64_e32 v[86:87], v[238:239]
	v_mov_b64_e32 v[88:89], v[232:233]
	v_mov_b64_e32 v[90:91], v[234:235]
	v_mov_b64_e32 v[92:93], v[236:237]
	v_mov_b64_e32 v[94:95], v[238:239]
	v_mov_b64_e32 v[96:97], v[232:233]
	v_mov_b64_e32 v[98:99], v[234:235]
	v_mov_b64_e32 v[100:101], v[228:229]
	v_mov_b64_e32 v[102:103], v[230:231]
	v_mov_b64_e32 v[104:105], v[224:225]
	v_mov_b64_e32 v[106:107], v[226:227]
	v_mov_b64_e32 v[108:109], v[228:229]
	v_mov_b64_e32 v[110:111], v[230:231]
	v_mov_b64_e32 v[112:113], v[224:225]
	v_mov_b64_e32 v[114:115], v[226:227]
	v_mov_b64_e32 v[116:117], v[228:229]
	v_mov_b64_e32 v[118:119], v[230:231]
	v_mov_b64_e32 v[120:121], v[224:225]
	v_mov_b64_e32 v[122:123], v[226:227]
	v_mov_b64_e32 v[124:125], v[228:229]
	v_mov_b64_e32 v[126:127], v[230:231]
	v_mov_b64_e32 v[128:129], v[224:225]
	v_mov_b64_e32 v[130:131], v[226:227]
	s_mov_b32 s76, s77
	s_andn2_b64 vcc, exec, s[38:39]
	s_cbranch_vccz .LBB0_1723

; template <class Epi, class Sched, bool ALIGN_EPI = false, bool SP2 = false, bool GATHER = false, bool HALFM = false>
; __device__ __forceinline__ void gemm_phase(PG8_LAS unsigned char* lds, const int Kdim, const Sched& S, const Epi& E) {
;     ...
;         for (int a = 0; a < 2; ++a)
; #pragma unroll
;             for (int b = 0; b < 2; ++b)
; #pragma unroll
;                 for (int m = 0; m < 4; ++m)
; #pragma unroll
;                     for (int n = 0; n < 2; ++n) acc[a][b][m][n] = (f32x4){0.f, 0.f, 0.f, 0.f};
;         cur = nxt; cA = nA; cB = nB; ++ui;
;     __device__ __forceinline__ void operator()(const pg8::f32x4 (&acc)[2][2][4][2], const pg8::Unit& u, int wr, int wc, int fr, int fq) const {
;     ...
;         const int col0 = u.pn * 256 + wc * 32 + 8 * fq;
;         f32x4 bv[2][2];
; #pragma unroll
;         for (int bj = 0; bj < 2; ++bj)
; #pragma unroll
;             for (int n = 0; n < 2; ++n) bv[bj][n] = *(const f32x4*)(b_down + u.e * 1024 + col0 + bj * 128 + 4 * n);
.LBB0_1816:
	s_and_b64 s[20:21], s[42:43], exec
	s_cselect_b32 s17, s39, s5
	s_cselect_b32 s36, s38, s4
	s_cselect_b32 s53, s41, s25
	s_cselect_b32 s54, s40, s24
	s_add_u32 s44, s4, 0x40080
	s_addc_u32 s45, s5, 0
	s_add_u32 s55, s24, 0x100
	s_waitcnt vmcnt(16)
	s_addc_u32 s56, s25, 0
	s_mov_b32 s57, -2
	v_mov_b64_e32 v[4:5], v[198:199]
	v_mov_b64_e32 v[6:7], v[200:201]
	v_mov_b64_e32 v[8:9], v[194:195]
	v_mov_b64_e32 v[10:11], v[196:197]
	v_mov_b64_e32 v[16:17], v[198:199]
	v_mov_b64_e32 v[18:19], v[200:201]
	v_mov_b64_e32 v[24:25], v[194:195]
	v_mov_b64_e32 v[26:27], v[196:197]
	v_mov_b64_e32 v[32:33], v[198:199]
	v_mov_b64_e32 v[34:35], v[200:201]
	v_mov_b64_e32 v[40:41], v[194:195]
	v_mov_b64_e32 v[42:43], v[196:197]
	v_mov_b64_e32 v[48:49], v[198:199]
	v_mov_b64_e32 v[50:51], v[200:201]
	v_mov_b64_e32 v[56:57], v[194:195]
	v_mov_b64_e32 v[58:59], v[196:197]
	v_mov_b64_e32 v[12:13], v[190:191]
	v_mov_b64_e32 v[14:15], v[192:193]
	v_mov_b64_e32 v[20:21], v[186:187]
	v_mov_b64_e32 v[22:23], v[188:189]
	v_mov_b64_e32 v[28:29], v[190:191]
	v_mov_b64_e32 v[30:31], v[192:193]
	v_mov_b64_e32 v[36:37], v[186:187]
	v_mov_b64_e32 v[38:39], v[188:189]
	v_mov_b64_e32 v[44:45], v[190:191]
	v_mov_b64_e32 v[46:47], v[192:193]
	v_mov_b64_e32 v[52:53], v[186:187]
	v_mov_b64_e32 v[54:55], v[188:189]
	v_mov_b64_e32 v[60:61], v[190:191]
	v_mov_b64_e32 v[62:63], v[192:193]
	v_mov_b64_e32 v[64:65], v[186:187]
	v_mov_b64_e32 v[66:67], v[188:189]
	v_mov_b64_e32 v[68:69], v[198:199]
	v_mov_b64_e32 v[70:71], v[200:201]
	v_mov_b64_e32 v[72:73], v[194:195]
	v_mov_b64_e32 v[74:75], v[196:197]
	v_mov_b64_e32 v[84:85], v[198:199]
	v_mov_b64_e32 v[86:87], v[200:201]
	v_mov_b64_e32 v[88:89], v[194:195]
	v_mov_b64_e32 v[90:91], v[196:197]
	v_mov_b64_e32 v[116:117], v[198:199]
	v_mov_b64_e32 v[118:119], v[200:201]
	v_mov_b64_e32 v[120:121], v[194:195]
	v_mov_b64_e32 v[122:123], v[196:197]
	v_mov_b64_e32 v[132:133], v[198:199]
	v_mov_b64_e32 v[134:135], v[200:201]
	v_mov_b64_e32 v[136:137], v[194:195]
	v_mov_b64_e32 v[138:139], v[196:197]
	v_mov_b64_e32 v[76:77], v[190:191]
	v_mov_b64_e32 v[78:79], v[192:193]
	v_mov_b64_e32 v[80:81], v[186:187]
	v_mov_b64_e32 v[82:83], v[188:189]
	v_mov_b64_e32 v[92:93], v[190:191]
	v_mov_b64_e32 v[94:95], v[192:193]
	v_mov_b64_e32 v[96:97], v[186:187]
	v_mov_b64_e32 v[98:99], v[188:189]
	v_mov_b64_e32 v[124:125], v[190:191]
	v_mov_b64_e32 v[126:127], v[192:193]
	v_mov_b64_e32 v[128:129], v[186:187]
	v_mov_b64_e32 v[130:131], v[188:189]
	v_mov_b64_e32 v[140:141], v[190:191]
	v_mov_b64_e32 v[142:143], v[192:193]
	v_mov_b64_e32 v[144:145], v[186:187]
	v_mov_b64_e32 v[146:147], v[188:189]
	s_cmp_eq_u32 s48, 1
	s_cbranch_scc1 .Ldn_unit_nobar
	s_cmp_eq_u64 s[0:1], 0
	s_cbranch_scc1 .Ldn_unit_nobar
	s_barrier
